# Grid barriers: non-leader workgroups poll the cross-XCD generation word directly (skips the leader's per-XCD release hop); each still does its own agent-scope acquire
# speedup vs baseline: 1.0182x; 1.0182x over previous
; __device__ __forceinline__ unsigned xb_ld(unsigned* p)              { return __hip_atomic_load(p, __ATOMIC_RELAXED, __HIP_MEMORY_SCOPE_AGENT); }
; __device__ __forceinline__ unsigned xb_add(unsigned* p, unsigned v) { return __hip_atomic_fetch_add(p, v, __ATOMIC_RELAXED, __HIP_MEMORY_SCOPE_AGENT); }
; #define XB_SPIN(cond, bar) do { unsigned _sp = 0; while (cond) { __builtin_amdgcn_s_sleep(1); \
;     if ((++_sp & 255u) == 0u) { if (xb_ld(&(bar)[XB_TMO])) break; if (_sp > XB_SPIN_CAP) { atomicAdd(&(bar)[XB_TMO], 1u); break; } } } } while (0)
; __device__ __forceinline__ void xcd_barrier(const XcdBarrier& b) {
;     ...
;         const unsigned old = xb_add(&bar[XB_XSUB(b.x)], 1u);
;         const unsigned gen = old / nloc;
;         if (old + 1u == (gen + 1u) * nloc) {
;             __builtin_amdgcn_fence(__ATOMIC_RELEASE, "agent");
;             asm volatile("s_waitcnt vmcnt(0)" ::: "memory");
;             const unsigned og = xb_add(&bar[XB_TOP], 1u);
;             const unsigned tg = og / nx;
;             if (og + 1u == (tg + 1u) * nx) xb_add(&bar[XB_TOPGEN], 1u);
;             else XB_SPIN(xb_ld(&bar[XB_TOPGEN]) == tg, bar);
;             __builtin_amdgcn_fence(__ATOMIC_ACQUIRE, "agent");
;             xb_add(&bar[XB_XGEN(b.x)], 1u);
;             asm volatile("s_waitcnt vmcnt(0)" ::: "memory");
;         } else {
;             XB_SPIN(xb_ld(&bar[XB_XGEN(b.x)]) == gen, bar);
;             __builtin_amdgcn_fence(__ATOMIC_ACQUIRE, "agent");
;             asm volatile("s_waitcnt vmcnt(0)" ::: "memory");
;         }
.LBB0_52:
	s_or_b64 exec, exec, s[8:9]
	v_cvt_f32_u32_e32 v5, v3
	s_waitcnt vmcnt(0)
	v_readfirstlane_b32 s6, v4
	s_add_u32 s4, s4, 0x2400
	s_addc_u32 s5, s5, 0
	v_rcp_iflag_f32_e32 v5, v5
	v_add_u32_e32 v6, s6, v2
	v_mul_f32_e32 v4, 0x4f7ffffe, v5
	v_cvt_u32_f32_e32 v4, v4
	v_sub_u32_e32 v5, 0, v3
	v_mul_lo_u32 v2, v5, v4
	v_mul_hi_u32 v2, v4, v2
	v_add_u32_e32 v2, v4, v2
	v_mul_hi_u32 v2, v6, v2
	v_mul_lo_u32 v4, v2, v3
	v_sub_u32_e32 v4, v6, v4
	v_add_u32_e32 v5, 1, v2
	v_cmp_ge_u32_e32 vcc, v4, v3
	s_nop 1
	v_cndmask_b32_e32 v2, v2, v5, vcc
	v_sub_u32_e32 v5, v4, v3
	v_cndmask_b32_e32 v4, v4, v5, vcc
	v_add_u32_e32 v5, 1, v2
	v_cmp_ge_u32_e32 vcc, v4, v3
	v_add_u32_e32 v4, 1, v6
	s_nop 0
	v_cndmask_b32_e32 v2, v2, v5, vcc
	v_mul_lo_u32 v5, v3, v2
	v_add_u32_e32 v3, v5, v3
	v_cmp_ne_u32_e32 vcc, v4, v3
	s_and_saveexec_b64 s[6:7], vcc
	s_xor_b64 s[6:7], exec, s[6:7]
	s_cbranch_execz .LBB0_66
	s_waitcnt lgkmcnt(0)
	v_readlane_b32 s100, v251, 25
	v_readlane_b32 s101, v251, 26
	s_add_u32 s100, s100, 0x7500
	s_addc_u32 s101, s101, 0
	v_mov_b32_e32 v1, 0
	global_load_dword v3, v1, s[100:101] sc1
	s_waitcnt vmcnt(0)
	v_cmp_eq_u32_e32 vcc, v3, v2
	s_and_saveexec_b64 s[8:9], vcc
	s_cbranch_execz .LBB0_65
	s_mov_b32 s33, 1
	s_mov_b64 s[10:11], 0
	s_branch .LBB0_56

; __device__ __forceinline__ unsigned xb_ld(unsigned* p)              { return __hip_atomic_load(p, __ATOMIC_RELAXED, __HIP_MEMORY_SCOPE_AGENT); }
; __device__ __forceinline__ unsigned xb_add(unsigned* p, unsigned v) { return __hip_atomic_fetch_add(p, v, __ATOMIC_RELAXED, __HIP_MEMORY_SCOPE_AGENT); }
; #define XB_SPIN(cond, bar) do { unsigned _sp = 0; while (cond) { __builtin_amdgcn_s_sleep(1); \
;     if ((++_sp & 255u) == 0u) { if (xb_ld(&(bar)[XB_TMO])) break; if (_sp > XB_SPIN_CAP) { atomicAdd(&(bar)[XB_TMO], 1u); break; } } } } while (0)
; __device__ __forceinline__ void xcd_barrier(const XcdBarrier& b) {
;     ...
;             else XB_SPIN(xb_ld(&bar[XB_TOPGEN]) == tg, bar);
;             __builtin_amdgcn_fence(__ATOMIC_ACQUIRE, "agent");
;             xb_add(&bar[XB_XGEN(b.x)], 1u);
;             asm volatile("s_waitcnt vmcnt(0)" ::: "memory");
;         } else {
;             XB_SPIN(xb_ld(&bar[XB_XGEN(b.x)]) == gen, bar);
.LBB0_60:
	global_load_dword v3, v1, s[100:101] sc1
	s_add_i32 s33, s33, 1
	s_mov_b64 s[24:25], -1
	s_waitcnt vmcnt(0)
	v_cmp_ne_u32_e32 vcc, v3, v2
	s_orn2_b64 s[16:17], vcc, exec
	s_branch .LBB0_55

; __device__ __forceinline__ unsigned xb_ld(unsigned* p)              { return __hip_atomic_load(p, __ATOMIC_RELAXED, __HIP_MEMORY_SCOPE_AGENT); }
; __device__ __forceinline__ unsigned xb_add(unsigned* p, unsigned v) { return __hip_atomic_fetch_add(p, v, __ATOMIC_RELAXED, __HIP_MEMORY_SCOPE_AGENT); }
; #define XB_SPIN(cond, bar) do { unsigned _sp = 0; while (cond) { __builtin_amdgcn_s_sleep(1); \
;     if ((++_sp & 255u) == 0u) { if (xb_ld(&(bar)[XB_TMO])) break; if (_sp > XB_SPIN_CAP) { atomicAdd(&(bar)[XB_TMO], 1u); break; } } } } while (0)
; __device__ __forceinline__ void xcd_barrier(const XcdBarrier& b) {
;     ...
;         const unsigned old = xb_add(&bar[XB_XSUB(b.x)], 1u);
;         const unsigned gen = old / nloc;
;         if (old + 1u == (gen + 1u) * nloc) {
;             __builtin_amdgcn_fence(__ATOMIC_RELEASE, "agent");
;             asm volatile("s_waitcnt vmcnt(0)" ::: "memory");
;             const unsigned og = xb_add(&bar[XB_TOP], 1u);
;             const unsigned tg = og / nx;
;             if (og + 1u == (tg + 1u) * nx) xb_add(&bar[XB_TOPGEN], 1u);
;             else XB_SPIN(xb_ld(&bar[XB_TOPGEN]) == tg, bar);
;             __builtin_amdgcn_fence(__ATOMIC_ACQUIRE, "agent");
;             xb_add(&bar[XB_XGEN(b.x)], 1u);
;             asm volatile("s_waitcnt vmcnt(0)" ::: "memory");
;         } else {
;             XB_SPIN(xb_ld(&bar[XB_XGEN(b.x)]) == gen, bar);
;             __builtin_amdgcn_fence(__ATOMIC_ACQUIRE, "agent");
;             asm volatile("s_waitcnt vmcnt(0)" ::: "memory");
;         }
.LBB0_261:
	s_or_b64 exec, exec, s[8:9]
	v_cvt_f32_u32_e32 v5, v3
	s_waitcnt vmcnt(0)
	v_readfirstlane_b32 s6, v4
	v_sub_u32_e32 v4, 0, v3
	v_rcp_iflag_f32_e32 v5, v5
	v_add_u32_e32 v6, s6, v2
	v_mul_f32_e32 v5, 0x4f7ffffe, v5
	v_cvt_u32_f32_e32 v5, v5
	v_mul_lo_u32 v2, v4, v5
	v_mul_hi_u32 v2, v5, v2
	v_add_u32_e32 v2, v5, v2
	v_mul_hi_u32 v2, v6, v2
	v_mul_lo_u32 v4, v2, v3
	v_sub_u32_e32 v4, v6, v4
	v_add_u32_e32 v5, 1, v2
	v_cmp_ge_u32_e32 vcc, v4, v3
	s_nop 1
	v_cndmask_b32_e32 v2, v2, v5, vcc
	v_sub_u32_e32 v5, v4, v3
	v_cndmask_b32_e32 v4, v4, v5, vcc
	v_add_u32_e32 v5, 1, v2
	v_cmp_ge_u32_e32 vcc, v4, v3
	v_add_u32_e32 v4, 1, v6
	s_nop 0
	v_cndmask_b32_e32 v2, v2, v5, vcc
	v_mul_lo_u32 v5, v3, v2
	v_add_u32_e32 v3, v5, v3
	v_cmp_ne_u32_e32 vcc, v4, v3
	s_and_saveexec_b64 s[6:7], vcc
	s_xor_b64 s[6:7], exec, s[6:7]
	s_cbranch_execz .LBB0_275
	s_waitcnt lgkmcnt(0)
	v_readlane_b32 s100, v251, 25
	v_readlane_b32 s101, v251, 26
	s_add_u32 s100, s100, 0x7500
	s_addc_u32 s101, s101, 0
	v_mov_b32_e32 v1, 0
	global_load_dword v1, v1, s[100:101] sc1
	s_add_u32 s16, s4, 0x2400
	s_addc_u32 s17, s5, 0
	s_waitcnt vmcnt(0)
	v_cmp_eq_u32_e32 vcc, v1, v2
	s_and_saveexec_b64 s[8:9], vcc
	s_cbranch_execz .LBB0_274
	s_add_u32 s14, s20, 0x4200
	s_addc_u32 s15, s21, 0
	s_mov_b32 s33, 1
	s_mov_b64 s[24:25], 0
	v_mov_b32_e32 v1, 0
	s_branch .LBB0_265

; __device__ __forceinline__ unsigned xb_ld(unsigned* p)              { return __hip_atomic_load(p, __ATOMIC_RELAXED, __HIP_MEMORY_SCOPE_AGENT); }
; __device__ __forceinline__ unsigned xb_add(unsigned* p, unsigned v) { return __hip_atomic_fetch_add(p, v, __ATOMIC_RELAXED, __HIP_MEMORY_SCOPE_AGENT); }
; #define XB_SPIN(cond, bar) do { unsigned _sp = 0; while (cond) { __builtin_amdgcn_s_sleep(1); \
;     if ((++_sp & 255u) == 0u) { if (xb_ld(&(bar)[XB_TMO])) break; if (_sp > XB_SPIN_CAP) { atomicAdd(&(bar)[XB_TMO], 1u); break; } } } } while (0)
; __device__ __forceinline__ void xcd_barrier(const XcdBarrier& b) {
;     ...
;             else XB_SPIN(xb_ld(&bar[XB_TOPGEN]) == tg, bar);
;             __builtin_amdgcn_fence(__ATOMIC_ACQUIRE, "agent");
;             xb_add(&bar[XB_XGEN(b.x)], 1u);
;             asm volatile("s_waitcnt vmcnt(0)" ::: "memory");
;         } else {
;             XB_SPIN(xb_ld(&bar[XB_XGEN(b.x)]) == gen, bar);
.LBB0_269:
	global_load_dword v3, v1, s[100:101] sc1
	s_add_i32 s33, s33, 1
	s_mov_b64 s[38:39], -1
	s_waitcnt vmcnt(0)
	v_cmp_ne_u32_e32 vcc, v3, v2
	s_orn2_b64 s[36:37], vcc, exec
	s_branch .LBB0_264

; __device__ __forceinline__ unsigned xb_ld(unsigned* p)              { return __hip_atomic_load(p, __ATOMIC_RELAXED, __HIP_MEMORY_SCOPE_AGENT); }
; __device__ __forceinline__ unsigned xb_add(unsigned* p, unsigned v) { return __hip_atomic_fetch_add(p, v, __ATOMIC_RELAXED, __HIP_MEMORY_SCOPE_AGENT); }
; #define XB_SPIN(cond, bar) do { unsigned _sp = 0; while (cond) { __builtin_amdgcn_s_sleep(1); \
;     if ((++_sp & 255u) == 0u) { if (xb_ld(&(bar)[XB_TMO])) break; if (_sp > XB_SPIN_CAP) { atomicAdd(&(bar)[XB_TMO], 1u); break; } } } } while (0)
; __device__ __forceinline__ void xcd_barrier(const XcdBarrier& b) {
;     ...
;         const unsigned old = xb_add(&bar[XB_XSUB(b.x)], 1u);
;         const unsigned gen = old / nloc;
;         if (old + 1u == (gen + 1u) * nloc) {
;             __builtin_amdgcn_fence(__ATOMIC_RELEASE, "agent");
;             asm volatile("s_waitcnt vmcnt(0)" ::: "memory");
;             const unsigned og = xb_add(&bar[XB_TOP], 1u);
;             const unsigned tg = og / nx;
;             if (og + 1u == (tg + 1u) * nx) xb_add(&bar[XB_TOPGEN], 1u);
;             else XB_SPIN(xb_ld(&bar[XB_TOPGEN]) == tg, bar);
;             __builtin_amdgcn_fence(__ATOMIC_ACQUIRE, "agent");
;             xb_add(&bar[XB_XGEN(b.x)], 1u);
;             asm volatile("s_waitcnt vmcnt(0)" ::: "memory");
;         } else {
;             XB_SPIN(xb_ld(&bar[XB_XGEN(b.x)]) == gen, bar);
;             __builtin_amdgcn_fence(__ATOMIC_ACQUIRE, "agent");
;             asm volatile("s_waitcnt vmcnt(0)" ::: "memory");
;         }
.LBB0_411:
	s_or_b64 exec, exec, s[8:9]
	v_cvt_f32_u32_e32 v5, v3
	s_waitcnt vmcnt(0)
	v_readfirstlane_b32 s6, v4
	v_sub_u32_e32 v4, 0, v3
	v_rcp_iflag_f32_e32 v5, v5
	v_add_u32_e32 v6, s6, v2
	v_mul_f32_e32 v5, 0x4f7ffffe, v5
	v_cvt_u32_f32_e32 v5, v5
	v_mul_lo_u32 v2, v4, v5
	v_mul_hi_u32 v2, v5, v2
	v_add_u32_e32 v2, v5, v2
	v_mul_hi_u32 v2, v6, v2
	v_mul_lo_u32 v4, v2, v3
	v_sub_u32_e32 v4, v6, v4
	v_add_u32_e32 v5, 1, v2
	v_cmp_ge_u32_e32 vcc, v4, v3
	s_nop 1
	v_cndmask_b32_e32 v2, v2, v5, vcc
	v_sub_u32_e32 v5, v4, v3
	v_cndmask_b32_e32 v4, v4, v5, vcc
	v_add_u32_e32 v5, 1, v2
	v_cmp_ge_u32_e32 vcc, v4, v3
	v_add_u32_e32 v4, 1, v6
	s_nop 0
	v_cndmask_b32_e32 v2, v2, v5, vcc
	v_mul_lo_u32 v5, v3, v2
	v_add_u32_e32 v3, v5, v3
	v_cmp_ne_u32_e32 vcc, v4, v3
	s_and_saveexec_b64 s[6:7], vcc
	s_xor_b64 s[6:7], exec, s[6:7]
	s_cbranch_execz .LBB0_425
	s_waitcnt lgkmcnt(0)
	v_readlane_b32 s100, v251, 25
	v_readlane_b32 s101, v251, 26
	s_add_u32 s100, s100, 0x7500
	s_addc_u32 s101, s101, 0
	v_mov_b32_e32 v1, 0
	global_load_dword v1, v1, s[100:101] sc1
	s_add_u32 s16, s4, 0x2400
	s_addc_u32 s17, s5, 0
	s_waitcnt vmcnt(0)
	v_cmp_eq_u32_e32 vcc, v1, v2
	s_and_saveexec_b64 s[8:9], vcc
	s_cbranch_execz .LBB0_424
	s_add_u32 s10, s36, 0x4200
	s_addc_u32 s11, s37, 0
	s_mov_b32 s33, 1
	s_mov_b64 s[24:25], 0
	v_mov_b32_e32 v1, 0
	s_branch .LBB0_415

; __device__ __forceinline__ unsigned xb_ld(unsigned* p)              { return __hip_atomic_load(p, __ATOMIC_RELAXED, __HIP_MEMORY_SCOPE_AGENT); }
; __device__ __forceinline__ unsigned xb_add(unsigned* p, unsigned v) { return __hip_atomic_fetch_add(p, v, __ATOMIC_RELAXED, __HIP_MEMORY_SCOPE_AGENT); }
; #define XB_SPIN(cond, bar) do { unsigned _sp = 0; while (cond) { __builtin_amdgcn_s_sleep(1); \
;     if ((++_sp & 255u) == 0u) { if (xb_ld(&(bar)[XB_TMO])) break; if (_sp > XB_SPIN_CAP) { atomicAdd(&(bar)[XB_TMO], 1u); break; } } } } while (0)
; __device__ __forceinline__ void xcd_barrier(const XcdBarrier& b) {
;     ...
;         const unsigned old = xb_add(&bar[XB_XSUB(b.x)], 1u);
;         const unsigned gen = old / nloc;
;         if (old + 1u == (gen + 1u) * nloc) {
;             __builtin_amdgcn_fence(__ATOMIC_RELEASE, "agent");
;             asm volatile("s_waitcnt vmcnt(0)" ::: "memory");
;             const unsigned og = xb_add(&bar[XB_TOP], 1u);
;             const unsigned tg = og / nx;
;             if (og + 1u == (tg + 1u) * nx) xb_add(&bar[XB_TOPGEN], 1u);
;             else XB_SPIN(xb_ld(&bar[XB_TOPGEN]) == tg, bar);
;             __builtin_amdgcn_fence(__ATOMIC_ACQUIRE, "agent");
;             xb_add(&bar[XB_XGEN(b.x)], 1u);
;             asm volatile("s_waitcnt vmcnt(0)" ::: "memory");
;         } else {
;             XB_SPIN(xb_ld(&bar[XB_XGEN(b.x)]) == gen, bar);
;             __builtin_amdgcn_fence(__ATOMIC_ACQUIRE, "agent");
;             asm volatile("s_waitcnt vmcnt(0)" ::: "memory");
;         }
.LBB0_469:
	s_or_b64 exec, exec, s[8:9]
	v_cvt_f32_u32_e32 v5, v3
	s_waitcnt vmcnt(0)
	v_readfirstlane_b32 s6, v4
	s_add_u32 s4, s4, 0x2400
	s_addc_u32 s5, s5, 0
	v_rcp_iflag_f32_e32 v5, v5
	v_add_u32_e32 v6, s6, v2
	v_mul_f32_e32 v4, 0x4f7ffffe, v5
	v_cvt_u32_f32_e32 v4, v4
	v_sub_u32_e32 v5, 0, v3
	v_mul_lo_u32 v2, v5, v4
	v_mul_hi_u32 v2, v4, v2
	v_add_u32_e32 v2, v4, v2
	v_mul_hi_u32 v2, v6, v2
	v_mul_lo_u32 v4, v2, v3
	v_sub_u32_e32 v4, v6, v4
	v_add_u32_e32 v5, 1, v2
	v_cmp_ge_u32_e32 vcc, v4, v3
	s_nop 1
	v_cndmask_b32_e32 v2, v2, v5, vcc
	v_sub_u32_e32 v5, v4, v3
	v_cndmask_b32_e32 v4, v4, v5, vcc
	v_add_u32_e32 v5, 1, v2
	v_cmp_ge_u32_e32 vcc, v4, v3
	v_add_u32_e32 v4, 1, v6
	s_nop 0
	v_cndmask_b32_e32 v2, v2, v5, vcc
	v_mul_lo_u32 v5, v3, v2
	v_add_u32_e32 v3, v5, v3
	v_cmp_ne_u32_e32 vcc, v4, v3
	s_and_saveexec_b64 s[6:7], vcc
	s_xor_b64 s[6:7], exec, s[6:7]
	s_cbranch_execz .LBB0_483
	s_waitcnt lgkmcnt(0)
	v_readlane_b32 s100, v251, 25
	v_readlane_b32 s101, v251, 26
	s_add_u32 s100, s100, 0x7500
	s_addc_u32 s101, s101, 0
	v_mov_b32_e32 v1, 0
	global_load_dword v3, v1, s[100:101] sc1
	s_waitcnt vmcnt(0)
	v_cmp_eq_u32_e32 vcc, v3, v2
	s_and_saveexec_b64 s[8:9], vcc
	s_cbranch_execz .LBB0_482
	s_mov_b32 s22, 1
	s_mov_b64 s[10:11], 0
	s_branch .LBB0_473

; __device__ __forceinline__ unsigned xb_ld(unsigned* p)              { return __hip_atomic_load(p, __ATOMIC_RELAXED, __HIP_MEMORY_SCOPE_AGENT); }
; __device__ __forceinline__ unsigned xb_add(unsigned* p, unsigned v) { return __hip_atomic_fetch_add(p, v, __ATOMIC_RELAXED, __HIP_MEMORY_SCOPE_AGENT); }
; #define XB_SPIN(cond, bar) do { unsigned _sp = 0; while (cond) { __builtin_amdgcn_s_sleep(1); \
;     if ((++_sp & 255u) == 0u) { if (xb_ld(&(bar)[XB_TMO])) break; if (_sp > XB_SPIN_CAP) { atomicAdd(&(bar)[XB_TMO], 1u); break; } } } } while (0)
; __device__ __forceinline__ void xcd_barrier(const XcdBarrier& b) {
;     ...
;             else XB_SPIN(xb_ld(&bar[XB_TOPGEN]) == tg, bar);
;             __builtin_amdgcn_fence(__ATOMIC_ACQUIRE, "agent");
;             xb_add(&bar[XB_XGEN(b.x)], 1u);
;             asm volatile("s_waitcnt vmcnt(0)" ::: "memory");
;         } else {
;             XB_SPIN(xb_ld(&bar[XB_XGEN(b.x)]) == gen, bar);
.LBB0_477:
	global_load_dword v3, v1, s[100:101] sc1
	s_add_i32 s22, s22, 1
	s_mov_b64 s[18:19], -1
	s_waitcnt vmcnt(0)
	v_cmp_ne_u32_e32 vcc, v3, v2
	s_orn2_b64 s[16:17], vcc, exec
	s_branch .LBB0_472

; __device__ __forceinline__ unsigned xb_ld(unsigned* p)              { return __hip_atomic_load(p, __ATOMIC_RELAXED, __HIP_MEMORY_SCOPE_AGENT); }
; __device__ __forceinline__ unsigned xb_add(unsigned* p, unsigned v) { return __hip_atomic_fetch_add(p, v, __ATOMIC_RELAXED, __HIP_MEMORY_SCOPE_AGENT); }
; #define XB_SPIN(cond, bar) do { unsigned _sp = 0; while (cond) { __builtin_amdgcn_s_sleep(1); \
;     if ((++_sp & 255u) == 0u) { if (xb_ld(&(bar)[XB_TMO])) break; if (_sp > XB_SPIN_CAP) { atomicAdd(&(bar)[XB_TMO], 1u); break; } } } } while (0)
; __device__ __forceinline__ void xcd_barrier(const XcdBarrier& b) {
;     ...
;         const unsigned old = xb_add(&bar[XB_XSUB(b.x)], 1u);
;         const unsigned gen = old / nloc;
;         if (old + 1u == (gen + 1u) * nloc) {
;             __builtin_amdgcn_fence(__ATOMIC_RELEASE, "agent");
;             asm volatile("s_waitcnt vmcnt(0)" ::: "memory");
;             const unsigned og = xb_add(&bar[XB_TOP], 1u);
;             const unsigned tg = og / nx;
;             if (og + 1u == (tg + 1u) * nx) xb_add(&bar[XB_TOPGEN], 1u);
;             else XB_SPIN(xb_ld(&bar[XB_TOPGEN]) == tg, bar);
;             __builtin_amdgcn_fence(__ATOMIC_ACQUIRE, "agent");
;             xb_add(&bar[XB_XGEN(b.x)], 1u);
;             asm volatile("s_waitcnt vmcnt(0)" ::: "memory");
;         } else {
;             XB_SPIN(xb_ld(&bar[XB_XGEN(b.x)]) == gen, bar);
;             __builtin_amdgcn_fence(__ATOMIC_ACQUIRE, "agent");
;             asm volatile("s_waitcnt vmcnt(0)" ::: "memory");
;         }
.LBB0_573:
	s_or_b64 exec, exec, s[8:9]
	v_cvt_f32_u32_e32 v5, v3
	s_waitcnt vmcnt(0)
	v_readfirstlane_b32 s6, v4
	s_add_u32 s4, s4, 0x2400
	s_addc_u32 s5, s5, 0
	v_rcp_iflag_f32_e32 v5, v5
	v_add_u32_e32 v6, s6, v2
	v_mul_f32_e32 v4, 0x4f7ffffe, v5
	v_cvt_u32_f32_e32 v4, v4
	v_sub_u32_e32 v5, 0, v3
	v_mul_lo_u32 v2, v5, v4
	v_mul_hi_u32 v2, v4, v2
	v_add_u32_e32 v2, v4, v2
	v_mul_hi_u32 v2, v6, v2
	v_mul_lo_u32 v4, v2, v3
	v_sub_u32_e32 v4, v6, v4
	v_add_u32_e32 v5, 1, v2
	v_cmp_ge_u32_e32 vcc, v4, v3
	s_nop 1
	v_cndmask_b32_e32 v2, v2, v5, vcc
	v_sub_u32_e32 v5, v4, v3
	v_cndmask_b32_e32 v4, v4, v5, vcc
	v_add_u32_e32 v5, 1, v2
	v_cmp_ge_u32_e32 vcc, v4, v3
	v_add_u32_e32 v4, 1, v6
	s_nop 0
	v_cndmask_b32_e32 v2, v2, v5, vcc
	v_mul_lo_u32 v5, v3, v2
	v_add_u32_e32 v3, v5, v3
	v_cmp_ne_u32_e32 vcc, v4, v3
	s_and_saveexec_b64 s[6:7], vcc
	s_xor_b64 s[6:7], exec, s[6:7]
	s_cbranch_execz .LBB0_587
	s_waitcnt lgkmcnt(0)
	v_readlane_b32 s100, v251, 25
	v_readlane_b32 s101, v251, 26
	s_add_u32 s100, s100, 0x7500
	s_addc_u32 s101, s101, 0
	v_mov_b32_e32 v1, 0
	global_load_dword v3, v1, s[100:101] sc1
	s_waitcnt vmcnt(0)
	v_cmp_eq_u32_e32 vcc, v3, v2
	s_and_saveexec_b64 s[8:9], vcc
	s_cbranch_execz .LBB0_586
	s_mov_b32 s20, 1
	s_mov_b64 s[10:11], 0
	s_branch .LBB0_577

; __device__ __forceinline__ unsigned xb_ld(unsigned* p)              { return __hip_atomic_load(p, __ATOMIC_RELAXED, __HIP_MEMORY_SCOPE_AGENT); }
; __device__ __forceinline__ unsigned xb_add(unsigned* p, unsigned v) { return __hip_atomic_fetch_add(p, v, __ATOMIC_RELAXED, __HIP_MEMORY_SCOPE_AGENT); }
; #define XB_SPIN(cond, bar) do { unsigned _sp = 0; while (cond) { __builtin_amdgcn_s_sleep(1); \
;     if ((++_sp & 255u) == 0u) { if (xb_ld(&(bar)[XB_TMO])) break; if (_sp > XB_SPIN_CAP) { atomicAdd(&(bar)[XB_TMO], 1u); break; } } } } while (0)
; __device__ __forceinline__ void xcd_barrier(const XcdBarrier& b) {
;     ...
;             else XB_SPIN(xb_ld(&bar[XB_TOPGEN]) == tg, bar);
;             __builtin_amdgcn_fence(__ATOMIC_ACQUIRE, "agent");
;             xb_add(&bar[XB_XGEN(b.x)], 1u);
;             asm volatile("s_waitcnt vmcnt(0)" ::: "memory");
;         } else {
;             XB_SPIN(xb_ld(&bar[XB_XGEN(b.x)]) == gen, bar);
.LBB0_581:
	global_load_dword v3, v1, s[100:101] sc1
	s_add_i32 s20, s20, 1
	s_mov_b64 s[16:17], -1
	s_waitcnt vmcnt(0)
	v_cmp_ne_u32_e32 vcc, v3, v2
	s_orn2_b64 s[14:15], vcc, exec
	s_branch .LBB0_576

; __device__ __forceinline__ unsigned xb_ld(unsigned* p)              { return __hip_atomic_load(p, __ATOMIC_RELAXED, __HIP_MEMORY_SCOPE_AGENT); }
; __device__ __forceinline__ unsigned xb_add(unsigned* p, unsigned v) { return __hip_atomic_fetch_add(p, v, __ATOMIC_RELAXED, __HIP_MEMORY_SCOPE_AGENT); }
; #define XB_SPIN(cond, bar) do { unsigned _sp = 0; while (cond) { __builtin_amdgcn_s_sleep(1); \
;     if ((++_sp & 255u) == 0u) { if (xb_ld(&(bar)[XB_TMO])) break; if (_sp > XB_SPIN_CAP) { atomicAdd(&(bar)[XB_TMO], 1u); break; } } } } while (0)
; __device__ __forceinline__ void xcd_barrier(const XcdBarrier& b) {
;     ...
;         const unsigned old = xb_add(&bar[XB_XSUB(b.x)], 1u);
;         const unsigned gen = old / nloc;
;         if (old + 1u == (gen + 1u) * nloc) {
;             __builtin_amdgcn_fence(__ATOMIC_RELEASE, "agent");
;             asm volatile("s_waitcnt vmcnt(0)" ::: "memory");
;             const unsigned og = xb_add(&bar[XB_TOP], 1u);
;             const unsigned tg = og / nx;
;             if (og + 1u == (tg + 1u) * nx) xb_add(&bar[XB_TOPGEN], 1u);
;             else XB_SPIN(xb_ld(&bar[XB_TOPGEN]) == tg, bar);
;             __builtin_amdgcn_fence(__ATOMIC_ACQUIRE, "agent");
;             xb_add(&bar[XB_XGEN(b.x)], 1u);
;             asm volatile("s_waitcnt vmcnt(0)" ::: "memory");
;         } else {
;             XB_SPIN(xb_ld(&bar[XB_XGEN(b.x)]) == gen, bar);
;             __builtin_amdgcn_fence(__ATOMIC_ACQUIRE, "agent");
;             asm volatile("s_waitcnt vmcnt(0)" ::: "memory");
;         }
.LBB0_655:
	s_or_b64 exec, exec, s[10:11]
	v_cvt_f32_u32_e32 v5, v3
	s_waitcnt vmcnt(0)
	v_readfirstlane_b32 s8, v4
	s_add_u32 s6, s6, 0x2400
	s_addc_u32 s7, s7, 0
	v_rcp_iflag_f32_e32 v5, v5
	v_add_u32_e32 v6, s8, v2
	v_mul_f32_e32 v4, 0x4f7ffffe, v5
	v_cvt_u32_f32_e32 v4, v4
	v_sub_u32_e32 v5, 0, v3
	v_mul_lo_u32 v2, v5, v4
	v_mul_hi_u32 v2, v4, v2
	v_add_u32_e32 v2, v4, v2
	v_mul_hi_u32 v2, v6, v2
	v_mul_lo_u32 v4, v2, v3
	v_sub_u32_e32 v4, v6, v4
	v_add_u32_e32 v5, 1, v2
	v_cmp_ge_u32_e32 vcc, v4, v3
	s_nop 1
	v_cndmask_b32_e32 v2, v2, v5, vcc
	v_sub_u32_e32 v5, v4, v3
	v_cndmask_b32_e32 v4, v4, v5, vcc
	v_add_u32_e32 v5, 1, v2
	v_cmp_ge_u32_e32 vcc, v4, v3
	v_add_u32_e32 v4, 1, v6
	s_nop 0
	v_cndmask_b32_e32 v2, v2, v5, vcc
	v_mul_lo_u32 v5, v3, v2
	v_add_u32_e32 v3, v5, v3
	v_cmp_ne_u32_e32 vcc, v4, v3
	s_and_saveexec_b64 s[8:9], vcc
	s_xor_b64 s[8:9], exec, s[8:9]
	s_cbranch_execz .LBB0_669
	s_waitcnt lgkmcnt(0)
	v_readlane_b32 s100, v251, 25
	v_readlane_b32 s101, v251, 26
	s_add_u32 s100, s100, 0x7500
	s_addc_u32 s101, s101, 0
	v_mov_b32_e32 v1, 0
	global_load_dword v3, v1, s[100:101] sc1
	s_waitcnt vmcnt(0)
	v_cmp_eq_u32_e32 vcc, v3, v2
	s_and_saveexec_b64 s[10:11], vcc
	s_cbranch_execz .LBB0_668
	s_mov_b32 s22, 1
	s_mov_b64 s[12:13], 0
	s_branch .LBB0_659

; __device__ __forceinline__ unsigned xb_ld(unsigned* p)              { return __hip_atomic_load(p, __ATOMIC_RELAXED, __HIP_MEMORY_SCOPE_AGENT); }
; __device__ __forceinline__ unsigned xb_add(unsigned* p, unsigned v) { return __hip_atomic_fetch_add(p, v, __ATOMIC_RELAXED, __HIP_MEMORY_SCOPE_AGENT); }
; #define XB_SPIN(cond, bar) do { unsigned _sp = 0; while (cond) { __builtin_amdgcn_s_sleep(1); \
;     if ((++_sp & 255u) == 0u) { if (xb_ld(&(bar)[XB_TMO])) break; if (_sp > XB_SPIN_CAP) { atomicAdd(&(bar)[XB_TMO], 1u); break; } } } } while (0)
; __device__ __forceinline__ void xcd_barrier(const XcdBarrier& b) {
;     ...
;         const unsigned old = xb_add(&bar[XB_XSUB(b.x)], 1u);
;         const unsigned gen = old / nloc;
;         if (old + 1u == (gen + 1u) * nloc) {
;             __builtin_amdgcn_fence(__ATOMIC_RELEASE, "agent");
;             asm volatile("s_waitcnt vmcnt(0)" ::: "memory");
;             const unsigned og = xb_add(&bar[XB_TOP], 1u);
;             const unsigned tg = og / nx;
;             if (og + 1u == (tg + 1u) * nx) xb_add(&bar[XB_TOPGEN], 1u);
;             else XB_SPIN(xb_ld(&bar[XB_TOPGEN]) == tg, bar);
;             __builtin_amdgcn_fence(__ATOMIC_ACQUIRE, "agent");
;             xb_add(&bar[XB_XGEN(b.x)], 1u);
;             asm volatile("s_waitcnt vmcnt(0)" ::: "memory");
;         } else {
;             XB_SPIN(xb_ld(&bar[XB_XGEN(b.x)]) == gen, bar);
;             __builtin_amdgcn_fence(__ATOMIC_ACQUIRE, "agent");
;             asm volatile("s_waitcnt vmcnt(0)" ::: "memory");
;         }
.LBB0_829:
	s_or_b64 exec, exec, s[10:11]
	v_cvt_f32_u32_e32 v5, v3
	s_waitcnt vmcnt(0)
	v_readfirstlane_b32 s8, v4
	s_add_u32 s4, s4, 0x2400
	s_addc_u32 s5, s5, 0
	v_rcp_iflag_f32_e32 v5, v5
	v_add_u32_e32 v6, s8, v2
	v_mul_f32_e32 v4, 0x4f7ffffe, v5
	v_cvt_u32_f32_e32 v4, v4
	v_sub_u32_e32 v5, 0, v3
	v_mul_lo_u32 v2, v5, v4
	v_mul_hi_u32 v2, v4, v2
	v_add_u32_e32 v2, v4, v2
	v_mul_hi_u32 v2, v6, v2
	v_mul_lo_u32 v4, v2, v3
	v_sub_u32_e32 v4, v6, v4
	v_add_u32_e32 v5, 1, v2
	v_cmp_ge_u32_e32 vcc, v4, v3
	s_nop 1
	v_cndmask_b32_e32 v2, v2, v5, vcc
	v_sub_u32_e32 v5, v4, v3
	v_cndmask_b32_e32 v4, v4, v5, vcc
	v_add_u32_e32 v5, 1, v2
	v_cmp_ge_u32_e32 vcc, v4, v3
	v_add_u32_e32 v4, 1, v6
	s_nop 0
	v_cndmask_b32_e32 v2, v2, v5, vcc
	v_mul_lo_u32 v5, v3, v2
	v_add_u32_e32 v3, v5, v3
	v_cmp_ne_u32_e32 vcc, v4, v3
	s_and_saveexec_b64 s[8:9], vcc
	s_xor_b64 s[8:9], exec, s[8:9]
	s_cbranch_execz .LBB0_843
	s_waitcnt lgkmcnt(0)
	v_readlane_b32 s100, v251, 25
	v_readlane_b32 s101, v251, 26
	s_add_u32 s100, s100, 0x7500
	s_addc_u32 s101, s101, 0
	v_mov_b32_e32 v1, 0
	global_load_dword v3, v1, s[100:101] sc1
	s_waitcnt vmcnt(0)
	v_cmp_eq_u32_e32 vcc, v3, v2
	s_and_saveexec_b64 s[10:11], vcc
	s_cbranch_execz .LBB0_842
	s_mov_b32 s22, 1
	s_mov_b64 s[12:13], 0
	s_branch .LBB0_833

; __device__ __forceinline__ unsigned xb_ld(unsigned* p)              { return __hip_atomic_load(p, __ATOMIC_RELAXED, __HIP_MEMORY_SCOPE_AGENT); }
; __device__ __forceinline__ unsigned xb_add(unsigned* p, unsigned v) { return __hip_atomic_fetch_add(p, v, __ATOMIC_RELAXED, __HIP_MEMORY_SCOPE_AGENT); }
; #define XB_SPIN(cond, bar) do { unsigned _sp = 0; while (cond) { __builtin_amdgcn_s_sleep(1); \
;     if ((++_sp & 255u) == 0u) { if (xb_ld(&(bar)[XB_TMO])) break; if (_sp > XB_SPIN_CAP) { atomicAdd(&(bar)[XB_TMO], 1u); break; } } } } while (0)
; __device__ __forceinline__ void xcd_barrier(const XcdBarrier& b) {
;     ...
;         const unsigned old = xb_add(&bar[XB_XSUB(b.x)], 1u);
;         const unsigned gen = old / nloc;
;         if (old + 1u == (gen + 1u) * nloc) {
;             __builtin_amdgcn_fence(__ATOMIC_RELEASE, "agent");
;             asm volatile("s_waitcnt vmcnt(0)" ::: "memory");
;             const unsigned og = xb_add(&bar[XB_TOP], 1u);
;             const unsigned tg = og / nx;
;             if (og + 1u == (tg + 1u) * nx) xb_add(&bar[XB_TOPGEN], 1u);
;             else XB_SPIN(xb_ld(&bar[XB_TOPGEN]) == tg, bar);
;             __builtin_amdgcn_fence(__ATOMIC_ACQUIRE, "agent");
;             xb_add(&bar[XB_XGEN(b.x)], 1u);
;             asm volatile("s_waitcnt vmcnt(0)" ::: "memory");
;         } else {
;             XB_SPIN(xb_ld(&bar[XB_XGEN(b.x)]) == gen, bar);
;             __builtin_amdgcn_fence(__ATOMIC_ACQUIRE, "agent");
;             asm volatile("s_waitcnt vmcnt(0)" ::: "memory");
;         }
.LBB0_932:
	s_or_b64 exec, exec, s[10:11]
	v_cvt_f32_u32_e32 v4, v2
	s_waitcnt vmcnt(0)
	v_readfirstlane_b32 s8, v3
	s_add_u32 s6, s6, 0x2400
	s_addc_u32 s7, s7, 0
	v_rcp_iflag_f32_e32 v4, v4
	v_add_u32_e32 v5, s8, v1
	v_mul_f32_e32 v3, 0x4f7ffffe, v4
	v_cvt_u32_f32_e32 v3, v3
	v_sub_u32_e32 v4, 0, v2
	v_mul_lo_u32 v1, v4, v3
	v_mul_hi_u32 v1, v3, v1
	v_add_u32_e32 v1, v3, v1
	v_mul_hi_u32 v1, v5, v1
	v_mul_lo_u32 v3, v1, v2
	v_sub_u32_e32 v3, v5, v3
	v_add_u32_e32 v4, 1, v1
	v_cmp_ge_u32_e32 vcc, v3, v2
	s_nop 1
	v_cndmask_b32_e32 v1, v1, v4, vcc
	v_sub_u32_e32 v4, v3, v2
	v_cndmask_b32_e32 v3, v3, v4, vcc
	v_add_u32_e32 v4, 1, v1
	v_cmp_ge_u32_e32 vcc, v3, v2
	v_add_u32_e32 v3, 1, v5
	s_nop 0
	v_cndmask_b32_e32 v1, v1, v4, vcc
	v_mul_lo_u32 v4, v2, v1
	v_add_u32_e32 v2, v4, v2
	v_cmp_ne_u32_e32 vcc, v3, v2
	s_and_saveexec_b64 s[8:9], vcc
	s_xor_b64 s[8:9], exec, s[8:9]
	s_cbranch_execz .LBB0_946
	s_waitcnt lgkmcnt(0)
	v_readlane_b32 s100, v251, 25
	v_readlane_b32 s101, v251, 26
	s_add_u32 s100, s100, 0x7500
	s_addc_u32 s101, s101, 0
	v_mov_b32_e32 v0, 0
	global_load_dword v2, v0, s[100:101] sc1
	s_waitcnt vmcnt(0)
	v_cmp_eq_u32_e32 vcc, v2, v1
	s_and_saveexec_b64 s[10:11], vcc
	s_cbranch_execz .LBB0_945
	s_mov_b32 s22, 1
	s_mov_b64 s[12:13], 0
	s_branch .LBB0_936

; __device__ __forceinline__ unsigned xb_ld(unsigned* p)              { return __hip_atomic_load(p, __ATOMIC_RELAXED, __HIP_MEMORY_SCOPE_AGENT); }
; __device__ __forceinline__ unsigned xb_add(unsigned* p, unsigned v) { return __hip_atomic_fetch_add(p, v, __ATOMIC_RELAXED, __HIP_MEMORY_SCOPE_AGENT); }
; #define XB_SPIN(cond, bar) do { unsigned _sp = 0; while (cond) { __builtin_amdgcn_s_sleep(1); \
;     if ((++_sp & 255u) == 0u) { if (xb_ld(&(bar)[XB_TMO])) break; if (_sp > XB_SPIN_CAP) { atomicAdd(&(bar)[XB_TMO], 1u); break; } } } } while (0)
; __device__ __forceinline__ void xcd_barrier(const XcdBarrier& b) {
;     ...
;             else XB_SPIN(xb_ld(&bar[XB_TOPGEN]) == tg, bar);
;             __builtin_amdgcn_fence(__ATOMIC_ACQUIRE, "agent");
;             xb_add(&bar[XB_XGEN(b.x)], 1u);
;             asm volatile("s_waitcnt vmcnt(0)" ::: "memory");
;         } else {
;             XB_SPIN(xb_ld(&bar[XB_XGEN(b.x)]) == gen, bar);
.LBB0_940:
	global_load_dword v2, v0, s[100:101] sc1
	s_add_i32 s22, s22, 1
	s_mov_b64 s[18:19], -1
	s_waitcnt vmcnt(0)
	v_cmp_ne_u32_e32 vcc, v2, v1
	s_orn2_b64 s[16:17], vcc, exec
	s_branch .LBB0_935
